# BEST + P1 row loop back edge skips the loop-top vmcnt waits (they only serialised on the previous row's write-through store acks)
# speedup vs baseline: 1.0070x; 1.0041x over previous
; __device__ __forceinline__ void p1_norm1(const Params& P, LAS unsigned char* lds, int tid, int blk, int G) {
;     ...
;         for (int rr = 0; rr < 8; ++rr) {
;             const int row = rb * 64 + wave * 8 + rr;
;             if (rr < 7) { const float* xn = P.in[0] + (size_t)(row + 1) * DM;
; #pragma unroll
;                 for (int i = 0; i < 8; ++i) vn[i] = *(const f32x4*)(xn + (i * 64 + lane) * 4); }
;             float ss = 0.f;
; #pragma unroll
;             for (int i = 0; i < 8; ++i) ss += v[i][0] * v[i][0] + v[i][1] * v[i][1] + v[i][2] * v[i][2] + v[i][3] * v[i][3];
;             ss = wave_sum(ss);
.LBB0_172:
	v_lshlrev_b64 v[2:3], 12, v[68:69]
	v_lshl_add_u64 v[88:89], v[82:83], 0, v[2:3]
	v_lshl_add_u64 v[90:91], v[84:85], 0, v[66:67]
	s_mov_b64 s[8:9], 0
	s_branch .LBB0_173
.Lp1_top2:
	v_mul_f32_e32 v79, v35, v35
	v_mul_f32_e32 v87, v39, v39
	v_mul_f32_e32 v120, v43, v43
	v_fmac_f32_e32 v79, v34, v34
	v_fmac_f32_e32 v87, v38, v38
	v_mul_f32_e32 v121, v47, v47
	v_pk_mul_f32 v[24:25], v[54:55], v[54:55]
	v_pk_mul_f32 v[98:99], v[50:51], v[50:51]
	v_fmac_f32_e32 v120, v42, v42
	v_fmac_f32_e32 v79, v36, v36
	v_fmac_f32_e32 v87, v40, v40
	v_pk_mul_f32 v[22:23], v[56:57], v[56:57]
	v_pk_mul_f32 v[94:95], v[52:53], v[52:53]
	v_mov_b32_e32 v110, v24
	v_mov_b32_e32 v111, v98
	v_mov_b32_e32 v98, v25
	v_fmac_f32_e32 v121, v46, v46
	v_fmac_f32_e32 v120, v44, v44
	v_fmac_f32_e32 v79, v37, v37
	v_fmac_f32_e32 v87, v41, v41
	s_branch .Lp1_body

; #define LAS __attribute__((address_space(3)))
; __device__ __forceinline__ unsigned cvt_pk_bf16(float lo, float hi) { const f32x2 v = {lo, hi}; return __builtin_bit_cast(unsigned, __builtin_convertvector(v, bf16x2_t)); }
; __device__ __forceinline__ void p1_norm1(const Params& P, LAS unsigned char* lds, int tid, int blk, int G) {
;     ...
;         for (int rr = 0; rr < 8; ++rr) {
;             const int row = rb * 64 + wave * 8 + rr;
;             if (rr < 7) { const float* xn = P.in[0] + (size_t)(row + 1) * DM;
; #pragma unroll
;                 for (int i = 0; i < 8; ++i) vn[i] = *(const f32x4*)(xn + (i * 64 + lane) * 4); }
;             float ss = 0.f;
; #pragma unroll
;             for (int i = 0; i < 8; ++i) ss += v[i][0] * v[i][0] + v[i][1] * v[i][1] + v[i][2] * v[i][2] + v[i][3] * v[i][3];
;             ss = wave_sum(ss);
;             const float r = rsqrtf(ss * (1.0f / 2048.0f) + 1e-6f);
; #pragma unroll
;             for (int i = 0; i < 8; ++i) {
;                 const int k = (i * 64 + lane) * 4;
;                 const f32x4 g4 = *(const LAS f32x4*)(gm + k), s4 = *(const LAS f32x4*)(sh + k);
;                 const f32x4 o = v[i] * r * g4 + s4;
;                 u32x2 w; w.x = cvt_pk_bf16(o[0], o[1]); w.y = cvt_pk_bf16(o[2], o[3]);
;                 __hip_atomic_store((unsigned long long*)(H + (size_t)row * DM + k), __builtin_bit_cast(unsigned long long, w), __ATOMIC_RELAXED, __HIP_MEMORY_SCOPE_AGENT);
;             }
; #pragma unroll
;             for (int i = 0; i < 8; ++i) v[i] = vn[i];
;         }
.Lp1_body:
	v_pk_mul_f32 v[20:21], v[62:63], v[62:63]
	v_pk_mul_f32 v[96:97], v[58:59], v[58:59]
	v_mov_b32_e32 v112, v22
	v_mov_b32_e32 v113, v94
	v_pk_add_f32 v[98:99], v[110:111], v[98:99]
	v_fmac_f32_e32 v121, v48, v48
	v_fmac_f32_e32 v120, v45, v45
	v_add_f32_e32 v79, v79, v87
	v_pk_mul_f32 v[18:19], v[64:65], v[64:65]
	v_pk_mul_f32 v[92:93], v[60:61], v[60:61]
	v_mov_b32_e32 v94, v23
	v_mov_b32_e32 v114, v20
	v_mov_b32_e32 v115, v96
	v_mov_b32_e32 v96, v21
	v_pk_add_f32 v[98:99], v[112:113], v[98:99]
	v_fmac_f32_e32 v121, v49, v49
	v_add_f32_e32 v79, v120, v79
	v_mov_b32_e32 v116, v18
	v_mov_b32_e32 v117, v92
	v_pk_add_f32 v[96:97], v[114:115], v[96:97]
	v_pk_add_f32 v[94:95], v[94:95], v[98:99]
	v_add_f32_e32 v79, v121, v79
	v_mov_b32_e32 v92, v19
	v_pk_add_f32 v[96:97], v[116:117], v[96:97]
	v_add_f32_e32 v79, v95, v79
	v_pk_add_f32 v[92:93], v[92:93], v[96:97]
	v_add_f32_e32 v79, v94, v79
	v_add_f32_e32 v79, v93, v79
	v_add_f32_e32 v79, v92, v79
	ds_bpermute_b32 v87, v100, v79
	v_add_co_u32_e32 v30, vcc, s28, v90
	v_lshl_add_u64 v[26:27], v[88:89], 0, s[8:9]
	s_nop 0
	v_addc_co_u32_e32 v31, vcc, 0, v91, vcc
	s_waitcnt lgkmcnt(0)
	v_add_f32_e32 v79, v79, v87
	ds_bpermute_b32 v87, v101, v79
	v_add_co_u32_e32 v118, vcc, s30, v26
	global_load_dwordx4 v[6:9], v[90:91], off offset:3072 nt
	global_load_dwordx4 v[10:13], v[90:91], off offset:2048 nt
	global_load_dwordx4 v[14:17], v[90:91], off offset:1024 nt
	global_load_dwordx4 v[2:5], v[90:91], off nt
	ds_read_b128 v[66:69], v106
	ds_read_b128 v[70:73], v106 offset:8192
	s_waitcnt lgkmcnt(2)
	v_add_f32_e32 v79, v79, v87
	ds_bpermute_b32 v87, v102, v79
	v_addc_co_u32_e32 v119, vcc, 0, v27, vcc
	global_load_dwordx4 v[18:21], v[30:31], off offset:3072 nt
	global_load_dwordx4 v[22:25], v[30:31], off offset:2048 nt
	global_load_dwordx4 v[26:29], v[30:31], off offset:1024 nt
	s_nop 0
	global_load_dwordx4 v[30:33], v[30:31], off nt
	s_waitcnt lgkmcnt(0)
	v_add_f32_e32 v79, v79, v87
	ds_bpermute_b32 v87, v103, v79
	s_add_u32 s8, s8, 0x1000
	s_addc_u32 s9, s9, 0
	v_lshl_add_u64 v[90:91], v[90:91], 0, s[4:5]
	s_cmpk_eq_i32 s8, 0x7000
	s_waitcnt lgkmcnt(0)
	v_add_f32_e32 v79, v79, v87
	ds_bpermute_b32 v87, v104, v79
	s_waitcnt lgkmcnt(0)
	v_add_f32_e32 v79, v79, v87
	ds_bpermute_b32 v87, v105, v79
	s_waitcnt lgkmcnt(0)
	v_add_f32_e32 v79, v79, v87
	v_fmamk_f32 v79, v79, 0x3a000000, v109
	v_mul_f32_e32 v87, 0x4b800000, v79
	v_cmp_gt_f32_e32 vcc, s29, v79
	s_nop 1
	v_cndmask_b32_e32 v79, v79, v87, vcc
	v_rsq_f32_e32 v79, v79
	s_nop 0
	v_mul_f32_e32 v87, 0x45800000, v79
	v_cndmask_b32_e32 v92, v79, v87, vcc
	v_pk_mul_f32 v[34:35], v[34:35], v[92:93] op_sel_hi:[1,0]
	v_pk_mul_f32 v[36:37], v[36:37], v[92:93] op_sel_hi:[1,0]
	v_pk_fma_f32 v[34:35], v[66:67], v[34:35], v[70:71]
	v_pk_fma_f32 v[36:37], v[68:69], v[36:37], v[72:73]
	v_cvt_pk_bf16_f32 v34, v34, v35
	v_cvt_pk_bf16_f32 v35, v36, v37
	global_store_dwordx2 v[118:119], v[34:35], off sc1
	v_pk_mul_f32 v[94:95], v[38:39], v[92:93] op_sel_hi:[1,0]
	v_pk_mul_f32 v[96:97], v[40:41], v[92:93] op_sel_hi:[1,0]
	ds_read_b128 v[34:37], v106 offset:1024
	ds_read_b128 v[38:41], v106 offset:9216
	v_pk_mul_f32 v[42:43], v[42:43], v[92:93] op_sel_hi:[1,0]
	v_pk_mul_f32 v[44:45], v[44:45], v[92:93] op_sel_hi:[1,0]
	v_pk_mul_f32 v[112:113], v[50:51], v[92:93] op_sel_hi:[1,0]
	v_pk_mul_f32 v[114:115], v[52:53], v[92:93] op_sel_hi:[1,0]
	s_waitcnt lgkmcnt(0)
	v_pk_fma_f32 v[36:37], v[36:37], v[96:97], v[40:41]
	v_pk_fma_f32 v[34:35], v[34:35], v[94:95], v[38:39]
	v_pk_mul_f32 v[116:117], v[54:55], v[92:93] op_sel_hi:[1,0]
	v_cvt_pk_bf16_f32 v34, v34, v35
	v_cvt_pk_bf16_f32 v35, v36, v37
	global_store_dwordx2 v[118:119], v[34:35], off offset:512 sc1
	ds_read_b128 v[34:37], v106 offset:2048
	ds_read_b128 v[38:41], v106 offset:10240
	v_pk_mul_f32 v[120:121], v[56:57], v[92:93] op_sel_hi:[1,0]
	v_pk_mul_f32 v[98:99], v[46:47], v[92:93] op_sel_hi:[1,0]
	v_pk_mul_f32 v[110:111], v[48:49], v[92:93] op_sel_hi:[1,0]
	v_pk_mul_f32 v[122:123], v[58:59], v[92:93] op_sel_hi:[1,0]
	s_waitcnt lgkmcnt(0)
	v_pk_fma_f32 v[36:37], v[36:37], v[44:45], v[40:41]
	v_pk_fma_f32 v[34:35], v[34:35], v[42:43], v[38:39]
	v_pk_mul_f32 v[124:125], v[60:61], v[92:93] op_sel_hi:[1,0]
	v_cvt_pk_bf16_f32 v34, v34, v35
	v_cvt_pk_bf16_f32 v35, v36, v37
	global_store_dwordx2 v[118:119], v[34:35], off offset:1024 sc1
	ds_read_b128 v[50:53], v106 offset:3072
	ds_read_b128 v[54:57], v106 offset:11264
	v_pk_mul_f32 v[126:127], v[62:63], v[92:93] op_sel_hi:[1,0]
	v_pk_mul_f32 v[92:93], v[64:65], v[92:93] op_sel_hi:[1,0]
	s_waitcnt lgkmcnt(0)
	v_pk_fma_f32 v[64:65], v[52:53], v[110:111], v[56:57]
	v_pk_fma_f32 v[66:67], v[50:51], v[98:99], v[54:55]
	s_waitcnt vmcnt(10)
	v_mov_b32_e32 v46, v6
	v_cvt_pk_bf16_f32 v66, v66, v67
	v_cvt_pk_bf16_f32 v67, v64, v65
	global_store_dwordx2 v[118:119], v[66:67], off offset:1536 sc1
	ds_read_b128 v[64:67], v106 offset:4096
	ds_read_b128 v[68:71], v106 offset:12288
	s_waitcnt vmcnt(8)
	v_mov_b32_e32 v34, v2
	v_mov_b32_e32 v35, v3
	v_mov_b32_e32 v36, v4
	v_mov_b32_e32 v37, v5
	s_waitcnt lgkmcnt(0)
	v_pk_fma_f32 v[66:67], v[66:67], v[114:115], v[70:71]
	v_pk_fma_f32 v[64:65], v[64:65], v[112:113], v[68:69]
	v_mov_b32_e32 v38, v14
	v_cvt_pk_bf16_f32 v64, v64, v65
	v_cvt_pk_bf16_f32 v65, v66, v67
	global_store_dwordx2 v[118:119], v[64:65], off offset:2048 sc1
	ds_read_b128 v[64:67], v106 offset:5120
	ds_read_b128 v[68:71], v106 offset:13312
	v_mov_b32_e32 v39, v15
	v_mov_b32_e32 v40, v16
	v_mov_b32_e32 v41, v17
	v_mov_b32_e32 v42, v10
	s_waitcnt lgkmcnt(0)
	v_pk_fma_f32 v[66:67], v[120:121], v[66:67], v[70:71]
	v_pk_fma_f32 v[64:65], v[116:117], v[64:65], v[68:69]
	v_mov_b32_e32 v43, v11
	v_cvt_pk_bf16_f32 v64, v64, v65
	v_cvt_pk_bf16_f32 v65, v66, v67
	global_store_dwordx2 v[118:119], v[64:65], off offset:2560 sc1
	ds_read_b128 v[64:67], v106 offset:6144
	ds_read_b128 v[68:71], v106 offset:14336
	v_mov_b32_e32 v44, v12
	v_mov_b32_e32 v45, v13
	v_mov_b32_e32 v47, v7
	v_mov_b32_e32 v48, v8
	s_waitcnt lgkmcnt(0)
	v_pk_fma_f32 v[66:67], v[124:125], v[66:67], v[70:71]
	v_pk_fma_f32 v[64:65], v[122:123], v[64:65], v[68:69]
	v_mov_b32_e32 v49, v9
	v_cvt_pk_bf16_f32 v64, v64, v65
	v_cvt_pk_bf16_f32 v65, v66, v67
	global_store_dwordx2 v[118:119], v[64:65], off offset:3072 sc1
	ds_read_b128 v[66:69], v106 offset:7168
	ds_read_b128 v[70:73], v106 offset:15360
	s_waitcnt vmcnt(7)
	v_mov_b32_e32 v50, v30
	v_mov_b32_e32 v51, v31
	v_mov_b32_e32 v52, v32
	v_mov_b32_e32 v53, v33
	s_waitcnt lgkmcnt(0)
	v_pk_fma_f32 v[68:69], v[92:93], v[68:69], v[72:73]
	v_pk_fma_f32 v[66:67], v[126:127], v[66:67], v[70:71]
	v_mov_b32_e32 v54, v26
	v_mov_b32_e32 v55, v27
	v_mov_b32_e32 v56, v28
	v_mov_b32_e32 v57, v29
	v_mov_b32_e32 v58, v22
	v_mov_b32_e32 v59, v23
	v_mov_b32_e32 v60, v24
	v_mov_b32_e32 v61, v25
	v_mov_b32_e32 v62, v18
	v_mov_b32_e32 v63, v19
	v_mov_b32_e32 v64, v20
	v_mov_b32_e32 v65, v21
	v_cvt_pk_bf16_f32 v66, v66, v67
	v_cvt_pk_bf16_f32 v67, v68, v69
	global_store_dwordx2 v[118:119], v[66:67], off offset:3584 sc1
	s_cbranch_scc0 .Lp1_top2
; #define LAS __attribute__((address_space(3)))
; __device__ __forceinline__ unsigned cvt_pk_bf16(float lo, float hi) { const f32x2 v = {lo, hi}; return __builtin_bit_cast(unsigned, __builtin_convertvector(v, bf16x2_t)); }
; __device__ __forceinline__ void p1_norm1(const Params& P, LAS unsigned char* lds, int tid, int blk, int G) {
;     ...
;         for (int rr = 0; rr < 8; ++rr) {
;             const int row = rb * 64 + wave * 8 + rr;
;             if (rr < 7) { const float* xn = P.in[0] + (size_t)(row + 1) * DM;
; #pragma unroll
;                 for (int i = 0; i < 8; ++i) vn[i] = *(const f32x4*)(xn + (i * 64 + lane) * 4); }
;             float ss = 0.f;
; #pragma unroll
;             for (int i = 0; i < 8; ++i) ss += v[i][0] * v[i][0] + v[i][1] * v[i][1] + v[i][2] * v[i][2] + v[i][3] * v[i][3];
;             ss = wave_sum(ss);
;             const float r = rsqrtf(ss * (1.0f / 2048.0f) + 1e-6f);
; #pragma unroll
;             for (int i = 0; i < 8; ++i) {
;                 const int k = (i * 64 + lane) * 4;
;                 const f32x4 g4 = *(const LAS f32x4*)(gm + k), s4 = *(const LAS f32x4*)(sh + k);
;                 const f32x4 o = v[i] * r * g4 + s4;
;                 u32x2 w; w.x = cvt_pk_bf16(o[0], o[1]); w.y = cvt_pk_bf16(o[2], o[3]);
;                 __hip_atomic_store((unsigned long long*)(H + (size_t)row * DM + k), __builtin_bit_cast(unsigned long long, w), __ATOMIC_RELAXED, __HIP_MEMORY_SCOPE_AGENT);
;             }
; #pragma unroll
;             for (int i = 0; i < 8; ++i) v[i] = vn[i];
;         }
;         __syncthreads();
	v_mul_f32_e32 v34, v3, v3
	v_mul_f32_e32 v35, v15, v15
	v_fmac_f32_e32 v34, v2, v2
	v_fmac_f32_e32 v35, v14, v14
	v_fmac_f32_e32 v34, v4, v4
	v_fmac_f32_e32 v35, v16, v16
	v_fmac_f32_e32 v34, v5, v5
	v_fmac_f32_e32 v35, v17, v17
	v_add_f32_e32 v34, v35, v34
	v_mul_f32_e32 v35, v11, v11
	v_fmac_f32_e32 v35, v10, v10
	v_fmac_f32_e32 v35, v12, v12
	v_fmac_f32_e32 v35, v13, v13
	v_add_f32_e32 v34, v35, v34
	v_mul_f32_e32 v35, v7, v7
	v_fmac_f32_e32 v35, v6, v6
	v_fmac_f32_e32 v35, v8, v8
	v_fmac_f32_e32 v35, v9, v9
	v_mov_b32_e32 v36, v27
	v_mov_b32_e32 v37, v31
	v_add_f32_e32 v38, v35, v34
	v_mov_b32_e32 v34, v26
	v_mov_b32_e32 v35, v30
	v_pk_mul_f32 v[36:37], v[36:37], v[36:37]
	v_ashrrev_i32_e32 v87, 31, v86
	v_pk_fma_f32 v[34:35], v[34:35], v[34:35], v[36:37]
	v_mov_b32_e32 v36, v28
	v_mov_b32_e32 v37, v32
	v_pk_fma_f32 v[34:35], v[36:37], v[36:37], v[34:35]
	v_mov_b32_e32 v36, v29
	v_mov_b32_e32 v37, v33
	v_pk_fma_f32 v[34:35], v[36:37], v[36:37], v[34:35]
	v_mov_b32_e32 v36, v19
	v_add_f32_e32 v35, v35, v38
	v_mov_b32_e32 v37, v23
	v_add_f32_e32 v38, v34, v35
	v_mov_b32_e32 v34, v18
	v_mov_b32_e32 v35, v22
	v_pk_mul_f32 v[36:37], v[36:37], v[36:37]
	v_lshlrev_b64 v[44:45], 12, v[86:87]
	v_pk_fma_f32 v[34:35], v[34:35], v[34:35], v[36:37]
	v_mov_b32_e32 v36, v20
	v_mov_b32_e32 v37, v24
	v_pk_fma_f32 v[34:35], v[36:37], v[36:37], v[34:35]
	v_mov_b32_e32 v36, v21
	v_mov_b32_e32 v37, v25
	v_pk_fma_f32 v[34:35], v[36:37], v[36:37], v[34:35]
	v_lshl_add_u64 v[44:45], v[80:81], 0, v[44:45]
	v_add_f32_e32 v35, v35, v38
	v_add_f32_e32 v34, v34, v35
	ds_bpermute_b32 v35, v100, v34
	s_add_i32 s34, s34, s33
	s_cmpk_gt_i32 s34, 0xff
	s_waitcnt lgkmcnt(0)
	v_add_f32_e32 v34, v34, v35
	ds_bpermute_b32 v35, v101, v34
	s_waitcnt lgkmcnt(0)
	v_add_f32_e32 v34, v34, v35
	ds_bpermute_b32 v35, v102, v34
	s_waitcnt lgkmcnt(0)
	v_add_f32_e32 v34, v34, v35
	ds_bpermute_b32 v35, v103, v34
	s_waitcnt lgkmcnt(0)
	v_add_f32_e32 v34, v34, v35
	ds_bpermute_b32 v35, v104, v34
	s_waitcnt lgkmcnt(0)
	v_add_f32_e32 v34, v34, v35
	ds_bpermute_b32 v35, v105, v34
	s_waitcnt lgkmcnt(0)
	v_add_f32_e32 v34, v34, v35
	v_fmamk_f32 v34, v34, 0x3a000000, v109
	v_mul_f32_e32 v35, 0x4b800000, v34
	v_cmp_gt_f32_e32 vcc, s29, v34
	s_nop 1
	v_cndmask_b32_e32 v34, v34, v35, vcc
	v_rsq_f32_e32 v34, v34
	s_nop 0
	v_mul_f32_e32 v35, 0x45800000, v34
	v_cndmask_b32_e32 v42, v34, v35, vcc
	ds_read_b128 v[34:37], v106
	ds_read_b128 v[38:41], v106 offset:8192
	v_pk_mul_f32 v[46:47], v[2:3], v[42:43] op_sel_hi:[1,0]
	v_pk_mul_f32 v[48:49], v[4:5], v[42:43] op_sel_hi:[1,0]
	s_waitcnt lgkmcnt(0)
	v_pk_fma_f32 v[34:35], v[34:35], v[46:47], v[38:39]
	v_pk_fma_f32 v[36:37], v[36:37], v[48:49], v[40:41]
	v_cvt_pk_bf16_f32 v34, v34, v35
	v_cvt_pk_bf16_f32 v35, v36, v37
	v_add_co_u32_e32 v36, vcc, s31, v44
	v_pk_mul_f32 v[46:47], v[14:15], v[42:43] op_sel_hi:[1,0]
	s_nop 0
	v_addc_co_u32_e32 v37, vcc, 0, v45, vcc
	global_store_dwordx2 v[36:37], v[34:35], off sc1
	ds_read_b128 v[34:37], v106 offset:1024
	ds_read_b128 v[38:41], v106 offset:9216
	v_pk_mul_f32 v[48:49], v[16:17], v[42:43] op_sel_hi:[1,0]
	v_lshl_add_u64 v[44:45], v[44:45], 0, s[6:7]
	s_waitcnt lgkmcnt(0)
	v_pk_fma_f32 v[36:37], v[36:37], v[48:49], v[40:41]
	v_pk_fma_f32 v[34:35], v[34:35], v[46:47], v[38:39]
	v_pk_mul_f32 v[46:47], v[10:11], v[42:43] op_sel_hi:[1,0]
	v_cvt_pk_bf16_f32 v34, v34, v35
	v_cvt_pk_bf16_f32 v35, v36, v37
	global_store_dwordx2 v[44:45], v[34:35], off offset:512 sc1
	ds_read_b128 v[34:37], v106 offset:2048
	ds_read_b128 v[38:41], v106 offset:10240
	v_pk_mul_f32 v[48:49], v[12:13], v[42:43] op_sel_hi:[1,0]
	s_waitcnt lgkmcnt(0)
	v_pk_fma_f32 v[34:35], v[34:35], v[46:47], v[38:39]
	v_pk_fma_f32 v[36:37], v[36:37], v[48:49], v[40:41]
	v_cvt_pk_bf16_f32 v34, v34, v35
	v_cvt_pk_bf16_f32 v35, v36, v37
	global_store_dwordx2 v[44:45], v[34:35], off offset:1024 sc1
	ds_read_b128 v[34:37], v106 offset:3072
	ds_read_b128 v[38:41], v106 offset:11264
	v_pk_mul_f32 v[46:47], v[6:7], v[42:43] op_sel_hi:[1,0]
	v_pk_mul_f32 v[48:49], v[8:9], v[42:43] op_sel_hi:[1,0]
	s_waitcnt lgkmcnt(0)
	v_pk_fma_f32 v[34:35], v[34:35], v[46:47], v[38:39]
	v_pk_fma_f32 v[36:37], v[36:37], v[48:49], v[40:41]
	v_cvt_pk_bf16_f32 v34, v34, v35
	v_cvt_pk_bf16_f32 v35, v36, v37
	global_store_dwordx2 v[44:45], v[34:35], off offset:1536 sc1
	ds_read_b128 v[34:37], v106 offset:4096
	ds_read_b128 v[38:41], v106 offset:12288
	v_pk_mul_f32 v[46:47], v[30:31], v[42:43] op_sel_hi:[1,0]
	v_pk_mul_f32 v[48:49], v[32:33], v[42:43] op_sel_hi:[1,0]
	s_waitcnt lgkmcnt(0)
	v_pk_fma_f32 v[34:35], v[46:47], v[34:35], v[38:39]
	v_pk_fma_f32 v[36:37], v[48:49], v[36:37], v[40:41]
	v_cvt_pk_bf16_f32 v34, v34, v35
	v_cvt_pk_bf16_f32 v35, v36, v37
	global_store_dwordx2 v[44:45], v[34:35], off offset:2048 sc1
	ds_read_b128 v[34:37], v106 offset:5120
	ds_read_b128 v[38:41], v106 offset:13312
	v_pk_mul_f32 v[46:47], v[26:27], v[42:43] op_sel_hi:[1,0]
	v_pk_mul_f32 v[48:49], v[28:29], v[42:43] op_sel_hi:[1,0]
	s_waitcnt lgkmcnt(0)
	v_pk_fma_f32 v[34:35], v[46:47], v[34:35], v[38:39]
	v_pk_fma_f32 v[36:37], v[48:49], v[36:37], v[40:41]
	v_cvt_pk_bf16_f32 v34, v34, v35
	v_cvt_pk_bf16_f32 v35, v36, v37
	global_store_dwordx2 v[44:45], v[34:35], off offset:2560 sc1
	ds_read_b128 v[34:37], v106 offset:6144
	ds_read_b128 v[38:41], v106 offset:14336
	v_pk_mul_f32 v[46:47], v[22:23], v[42:43] op_sel_hi:[1,0]
	v_pk_mul_f32 v[48:49], v[24:25], v[42:43] op_sel_hi:[1,0]
	s_waitcnt lgkmcnt(0)
	v_pk_fma_f32 v[34:35], v[46:47], v[34:35], v[38:39]
	v_pk_fma_f32 v[36:37], v[48:49], v[36:37], v[40:41]
	v_cvt_pk_bf16_f32 v34, v34, v35
	v_cvt_pk_bf16_f32 v35, v36, v37
	global_store_dwordx2 v[44:45], v[34:35], off offset:3072 sc1
	ds_read_b128 v[34:37], v106 offset:7168
	ds_read_b128 v[38:41], v106 offset:15360
	v_pk_mul_f32 v[46:47], v[18:19], v[42:43] op_sel_hi:[1,0]
	v_pk_mul_f32 v[42:43], v[20:21], v[42:43] op_sel_hi:[1,0]
	s_waitcnt lgkmcnt(0)
	v_pk_fma_f32 v[34:35], v[46:47], v[34:35], v[38:39]
	v_pk_fma_f32 v[36:37], v[42:43], v[36:37], v[40:41]
	v_cvt_pk_bf16_f32 v34, v34, v35
	v_cvt_pk_bf16_f32 v35, v36, v37
	global_store_dwordx2 v[44:45], v[34:35], off offset:3584 sc1
	s_barrier
	s_cbranch_scc0 .LBB0_166
